# MoBA loop: first half-step barrier moved ahead of the row-max tree (LDS reads already complete there)
# speedup vs baseline: 1.0119x; 1.0119x over previous
;     float pmax;
;     { float m0 = fmaxf(p0[0], p0[1]), m1 = fmaxf(p0[2], p0[3]), m2 = fmaxf(p1[0], p1[1]), m3 = fmaxf(p1[2], p1[3]);
; #pragma unroll
;       for (int r = 4; r < 16; r += 4) { m0 = fmaxf(fmaxf(m0, p0[r]), p0[r + 1]); m1 = fmaxf(fmaxf(m1, p0[r + 2]), p0[r + 3]); m2 = fmaxf(fmaxf(m2, p1[r]), p1[r + 1]); m3 = fmaxf(fmaxf(m3, p1[r + 2]), p1[r + 3]); }
;       pmax = fmaxf(fmaxf(m0, m1), fmaxf(m2, m3)); }
;     pmax = dead ? -__builtin_inff() : pmax;
;     { auto rr = __builtin_amdgcn_permlane32_swap(__float_as_uint(pmax), __float_as_uint(pmax), false, false);
;       pmax = fmaxf(__uint_as_float(rr[0]), __uint_as_float(rr[1])); }
;     constexpr float SCL = SCALE / (float)(1 << SH), C2 = 1.4426950408889634f * SCL;
;     if (__builtin_expect(__all((pmax - m_reg) * SCL <= (float)THRI), 1)) { mn = m_reg; alpha = 1.f; }
;     else { mn = fmaxf(m_reg, pmax); alpha = __builtin_amdgcn_exp2f((m_reg - mn) * C2); m_reg = mn; }
.LBB0_1045:
	s_barrier
	s_add_i32 s8, s90, 0xffffff80
	s_cmp_lt_u32 s8, s72
	s_cselect_b64 s[6:7], -1, 0
	s_lshr_b32 s8, s8, 8
	s_lshl_b32 s8, 1, s8
	v_and_b32_e32 v13, s8, v131
	v_cmp_eq_u32_e32 vcc, 0, v13
	v_max_f32_e32 v13, v99, v99
	v_max_f32_e32 v15, v98, v98
	v_max_f32_e32 v13, v15, v13
	v_max_f32_e32 v15, v101, v101
	v_max_f32_e32 v16, v100, v100
	v_max_f32_e32 v15, v16, v15
	v_max_f32_e32 v16, v85, v85
	v_max_f32_e32 v17, v84, v84
	v_max_f32_e32 v16, v17, v16
	v_max3_f32 v17, v82, v83, v86
	v_max3_f32 v16, v16, v88, v89
	v_max3_f32 v13, v13, v102, v103
	v_max3_f32 v15, v15, v104, v105
	v_max3_f32 v17, v17, v87, v90
	v_max3_f32 v16, v16, v92, v93
	v_max3_f32 v13, v13, v106, v107
	v_max3_f32 v15, v15, v108, v109
	v_max3_f32 v17, v17, v91, v94
	v_max3_f32 v16, v16, v96, v97
	v_max3_f32 v13, v13, v110, v111
	v_max3_f32 v15, v15, v112, v113
	v_max3_f32 v16, v17, v95, v16
	v_max3_f32 v13, v13, v15, v16
	s_and_b64 s[6:7], s[6:7], vcc
	v_cndmask_b32_e64 v13, v13, v210, s[6:7]
	v_mov_b32_e32 v15, v13
	s_nop 1
	v_permlane32_swap_b32_e32 v13, v15
	v_max_f32_e32 v15, v15, v15
	v_max_f32_e32 v13, v13, v13
	v_max_f32_e32 v13, v13, v15
	v_max_f32_e32 v16, v163, v163
	v_sub_f32_e32 v15, v13, v163
	v_max_f32_e32 v13, v16, v13
	v_sub_f32_e32 v16, v163, v13
	v_mul_f32_e32 v16, 0x3a0293ee, v16
	v_mul_f32_e32 v15, 0x39b504f3, v15
	v_exp_f32_e32 v16, v16
	v_cmp_ge_f32_e32 vcc, 2.0, v15
	s_cmp_eq_u64 vcc, exec
	s_cselect_b64 s[8:9], -1, 0
	s_waitcnt vmcnt(0)
	v_cndmask_b32_e64 v15, v16, 1.0, s[8:9]
	v_cmp_gt_f32_e32 vcc, 1.0, v15
	s_waitcnt vmcnt(1)
	ds_write_b128 v160, v[4:7]
	s_waitcnt vmcnt(0)
	ds_write_b128 v161, v[8:11] offset:32768
	s_cbranch_vccz .LBB0_1049
	s_and_saveexec_b64 s[10:11], s[4:5]
	ds_write_b32 v155, v15 offset:128
	s_or_b64 exec, exec, s[10:11]
	s_waitcnt lgkmcnt(0)
	v_add_u32_e32 v16, s73, v154
	ds_read_b128 v[136:139], v16 offset:224
	ds_read_b128 v[140:143], v16 offset:192
	ds_read_b128 v[144:147], v16 offset:160
	ds_read_b128 v[148:151], v16 offset:128
	s_waitcnt lgkmcnt(3)
	v_pk_mul_f32 v[46:47], v[46:47], v[136:137]
	s_waitcnt lgkmcnt(2)
	v_pk_mul_f32 v[42:43], v[42:43], v[140:141]
	s_waitcnt lgkmcnt(1)
	v_pk_mul_f32 v[38:39], v[38:39], v[144:145]
	v_pk_mul_f32 v[48:49], v[48:49], v[138:139]
	v_pk_mul_f32 v[44:45], v[44:45], v[142:143]
	v_pk_mul_f32 v[40:41], v[40:41], v[146:147]
	s_waitcnt lgkmcnt(0)
	v_pk_mul_f32 v[36:37], v[36:37], v[150:151]
	v_pk_mul_f32 v[34:35], v[34:35], v[148:149]
	v_pk_mul_f32 v[62:63], v[62:63], v[136:137]
	v_pk_mul_f32 v[58:59], v[58:59], v[140:141]
	v_pk_mul_f32 v[54:55], v[54:55], v[144:145]
	v_pk_mul_f32 v[64:65], v[64:65], v[138:139]
	v_pk_mul_f32 v[60:61], v[60:61], v[142:143]
	v_pk_mul_f32 v[56:57], v[56:57], v[146:147]
	v_pk_mul_f32 v[52:53], v[52:53], v[150:151]
	v_pk_mul_f32 v[50:51], v[50:51], v[148:149]
	v_pk_mul_f32 v[30:31], v[30:31], v[136:137]
	v_pk_mul_f32 v[26:27], v[26:27], v[140:141]
	v_pk_mul_f32 v[22:23], v[22:23], v[144:145]
	v_pk_mul_f32 v[32:33], v[32:33], v[138:139]
	v_pk_mul_f32 v[28:29], v[28:29], v[142:143]
	v_pk_mul_f32 v[24:25], v[24:25], v[146:147]
	v_pk_mul_f32 v[20:21], v[20:21], v[150:151]
	v_pk_mul_f32 v[18:19], v[18:19], v[148:149]
	v_pk_mul_f32 v[78:79], v[78:79], v[136:137]
	v_pk_mul_f32 v[74:75], v[74:75], v[140:141]
	v_pk_mul_f32 v[70:71], v[70:71], v[144:145]
	v_pk_mul_f32 v[80:81], v[80:81], v[138:139]
	v_pk_mul_f32 v[76:77], v[76:77], v[142:143]
	v_pk_mul_f32 v[72:73], v[72:73], v[146:147]
	v_pk_mul_f32 v[68:69], v[68:69], v[150:151]
	v_pk_mul_f32 v[66:67], v[66:67], v[148:149]

;     float pmax;
;     { float m0 = fmaxf(p0[0], p0[1]), m1 = fmaxf(p0[2], p0[3]), m2 = fmaxf(p1[0], p1[1]), m3 = fmaxf(p1[2], p1[3]);
; #pragma unroll
;       for (int r = 4; r < 16; r += 4) { m0 = fmaxf(fmaxf(m0, p0[r]), p0[r + 1]); m1 = fmaxf(fmaxf(m1, p0[r + 2]), p0[r + 3]); m2 = fmaxf(fmaxf(m2, p1[r]), p1[r + 1]); m3 = fmaxf(fmaxf(m3, p1[r + 2]), p1[r + 3]); }
;       pmax = fmaxf(fmaxf(m0, m1), fmaxf(m2, m3)); }
;     pmax = dead ? -__builtin_inff() : pmax;
;     { auto rr = __builtin_amdgcn_permlane32_swap(__float_as_uint(pmax), __float_as_uint(pmax), false, false);
;       pmax = fmaxf(__uint_as_float(rr[0]), __uint_as_float(rr[1])); }
;     constexpr float SCL = SCALE / (float)(1 << SH), C2 = 1.4426950408889634f * SCL;
;     if (__builtin_expect(__all((pmax - m_reg) * SCL <= (float)THRI), 1)) { mn = m_reg; alpha = 1.f; }
.LBB0_1053:
	s_barrier
	s_cmp_lt_u32 s86, s72
	s_cselect_b64 s[6:7], -1, 0
	s_lshr_b32 s8, s81, 2
	s_lshl_b32 s8, 1, s8
	v_and_b32_e32 v12, s8, v131
	v_cmp_eq_u32_e32 vcc, 0, v12
	v_max_f32_e32 v12, v99, v99
	v_max_f32_e32 v13, v98, v98
	v_max_f32_e32 v12, v13, v12
	v_max_f32_e32 v13, v101, v101
	v_max_f32_e32 v136, v100, v100
	v_max_f32_e32 v13, v136, v13
	v_max_f32_e32 v136, v85, v85
	v_max_f32_e32 v137, v84, v84
	v_max_f32_e32 v136, v137, v136
	v_max3_f32 v137, v82, v83, v86
	v_max3_f32 v136, v136, v88, v89
	v_max3_f32 v12, v12, v102, v103
	v_max3_f32 v13, v13, v104, v105
	v_max3_f32 v137, v137, v87, v90
	v_max3_f32 v136, v136, v92, v93
	v_max3_f32 v12, v12, v106, v107
	v_max3_f32 v13, v13, v108, v109
	v_max3_f32 v137, v137, v91, v94
	v_max3_f32 v136, v136, v96, v97
	v_max3_f32 v12, v12, v110, v111
	v_max3_f32 v13, v13, v112, v113
	v_max3_f32 v136, v137, v95, v136
	v_max3_f32 v12, v12, v13, v136
	s_and_b64 s[6:7], s[6:7], vcc
	v_cndmask_b32_e64 v12, v12, v210, s[6:7]
	v_mov_b32_e32 v13, v12
	s_nop 1
	v_permlane32_swap_b32_e32 v12, v13
	v_max_f32_e32 v13, v13, v13
	v_max_f32_e32 v12, v12, v12
	v_max_f32_e32 v12, v12, v13
	v_sub_f32_e32 v13, v12, v16
	v_mul_f32_e32 v13, 0x39b504f3, v13
	v_cmp_ge_f32_e32 vcc, 2.0, v13
	s_cmp_eq_u64 vcc, exec
	s_cselect_b64 s[8:9], -1, 0
	s_andn2_b64 vcc, exec, s[70:71]
	s_cbranch_vccnz .LBB0_1055
	s_waitcnt vmcnt(0)
	s_waitcnt vmcnt(1)
	ds_write_b128 v160, v[4:7] offset:16384
	s_waitcnt vmcnt(0)
	ds_write_b128 v161, v[8:11] offset:49152
